# P7 swiglu epilogue with packed f32 math (same ops, same order) + ragged MoE tiles skip the MFMAs of an all-padding second row half in P7
# speedup vs baseline: 1.0056x; 1.0056x over previous
.LBB0_1027:
	s_ashr_i32 s5, s5, 8
	s_add_i32 s80, s5, s4
	v_ashrrev_i32_e32 v1, 6, v0
	s_lshl_b32 s4, s14, 13
	v_and_b32_e32 v2, 48, v0
	v_lshl_add_u32 v3, v1, 10, s4
	v_lshlrev_b32_e32 v4, 6, v0
	s_movk_i32 s4, 0x3c0
	v_and_or_b32 v2, v4, s4, v2
	v_readlane_b32 s4, v255, 28
	s_lshl_b32 s4, s4, 5
	s_and_b32 s45, s4, 0x60
	s_lshl_b32 s44, s14, 6
	s_lshr_b32 s4, s45, 3
	s_add_u32 s14, s90, 0x31100000
	s_addc_u32 s15, s91, 0
	v_add_lshl_u32 v1, v1, s4, 10
	s_add_u32 s4, s50, 0x80
	s_waitcnt vmcnt(2)
	s_barrier
	s_addc_u32 s5, s51, 0
	s_add_i32 s46, s2, 0x18000
	s_mov_b32 s16, m0
	s_mov_b32 m0, s46
	s_nop 2
	global_load_lds_dwordx4 v252, s[4:5]
	s_mov_b32 m0, s16
	s_add_i32 s48, s2, 0x1a000
	s_mov_b32 s16, m0
	s_mov_b32 m0, s48
	s_nop 2
	global_load_lds_dwordx4 v253, s[4:5]
	s_mov_b32 m0, s16
	s_add_u32 s4, s90, 0xd100080
	s_addc_u32 s5, s91, 0
	s_add_i32 s49, s2, 0x8000
	s_mov_b32 s16, m0
	s_mov_b32 m0, s49
	s_nop 2
	global_load_lds_dwordx4 v36, s[4:5]
	s_mov_b32 m0, s16
	s_add_i32 s52, s2, 0xa000
	s_mov_b32 s16, m0
	s_mov_b32 m0, s52
	s_nop 2
	global_load_lds_dwordx4 v37, s[4:5]
	s_mov_b32 m0, s16
	s_add_u32 s4, s50, 0x400080
	s_addc_u32 s5, s51, 0
	s_add_i32 s53, s2, 0x1c000
	s_mov_b32 s16, m0
	s_mov_b32 m0, s53
	s_nop 2
	global_load_lds_dwordx4 v252, s[4:5]
	s_mov_b32 m0, s16
	v_lshlrev_b32_e32 v0, 2, v0
	s_add_i32 s54, s2, 0x1e000
	s_mov_b32 s16, m0
	s_mov_b32 m0, s54
	s_nop 2
	global_load_lds_dwordx4 v253, s[4:5]
	s_mov_b32 m0, s16
	v_and_b32_e32 v0, 32, v0
	s_waitcnt vmcnt(6)
	s_add_i32 s55, s2, 0xc000
	v_readlane_b32 s4, v255, 0
	v_bitop3_b32 v3, v2, v3, v0 bitop3:0xde
	v_bitop3_b32 v0, v2, v1, v0 bitop3:0xde
	s_cmpk_lt_u32 s4, 0x100
	s_mov_b32 s47, 0
	s_cselect_b64 s[16:17], -1, 0
	s_add_i32 s74, s2, 0xe000
	v_add_u32_e32 v254, 0, v0
	v_add_u32_e32 v152, 0, v3
	v_mov_b32_e32 v153, 0x7f7f7f7f
	s_mov_b32 s75, 0xc0e00000
	v_mov_b32_e32 v154, 0x40e00000
	s_mov_b64 s[36:37], s[8:9]
	s_barrier
	s_mov_b32 s32, 0
	s_branch .LBB0_1030

.LBB0_1029:
	v_readlane_b32 vcc_lo, v255, 28
	s_lshr_b32 vcc_lo, vcc_lo, 2
	s_lshl_b32 vcc_lo, vcc_lo, 6
	s_addk_i32 vcc_lo, 0x80
	s_cmp_le_i32 s78, vcc_lo
	s_cselect_b32 s32, 1, 0
	s_andn2_b64 vcc, exec, s[4:5]
	s_mov_b64 s[36:37], s[8:9]
	s_mov_b64 s[50:51], s[20:21]
	s_mov_b32 s24, s76
	s_mov_b32 s26, s18
	s_mov_b32 s80, s79
	s_mov_b64 s[56:57], s[22:23]
	s_cbranch_vccz .LBB0_1044

.LBB0_1036:
	s_add_u32 s50, s36, 0x100
	s_addc_u32 s51, s37, 0
	s_and_b64 s[56:57], s[58:59], exec
	s_cselect_b32 s64, s30, s19
	s_cselect_b32 s65, s31, s25
	s_cselect_b32 s63, s29, s82
	s_cselect_b32 s62, s28, s81
	s_add_u32 s56, s64, 0x80
	v_add_u32_e32 v144, 0x10000, v254
	s_addc_u32 s57, s65, 0
	ds_read_b128 v[116:119], v144
	ds_read_b128 v[120:123], v144 offset:1024
	ds_read_b128 v[156:159], v144 offset:2048
	ds_read_b128 v[160:163], v144 offset:3072
	v_add_u32_e32 v144, 0x14000, v254
	s_add_u32 s72, s36, 0x80
	ds_read_b128 v[164:167], v144
	ds_read_b128 v[168:171], v144 offset:1024
	ds_read_b128 v[172:175], v144 offset:2048
	ds_read_b128 v[176:179], v144 offset:3072
	s_addc_u32 s73, s37, 0
	s_and_b64 s[36:37], s[58:59], exec
	s_cselect_b32 s60, s34, s50
	s_cselect_b32 s61, s35, s51
	s_add_u32 s36, s60, 0x80
	s_addc_u32 s37, s61, 0
	s_add_u32 s58, s62, 0x80
	s_addc_u32 s59, s63, 0
	ds_read_b128 v[180:183], v152
	ds_read_b128 v[184:187], v152 offset:1024
	ds_read_b128 v[188:191], v152 offset:2048
	ds_read_b128 v[192:195], v152 offset:3072
	ds_read_b128 v[196:199], v152 offset:4096
	ds_read_b128 v[200:203], v152 offset:5120
	ds_read_b128 v[204:207], v152 offset:6144
	ds_read_b128 v[208:211], v152 offset:7168
	s_mov_b32 s84, m0
	s_mov_b32 m0, s55
	s_nop 2
	global_load_lds_dwordx4 v38, s[72:73]
	s_mov_b32 m0, s84
	s_nop 0
	s_mov_b32 s84, m0
	s_mov_b32 m0, s74
	s_nop 2
	global_load_lds_dwordx4 v39, s[72:73]
	s_mov_b32 m0, s84
	s_waitcnt vmcnt(8)
	s_waitcnt lgkmcnt(0)
	s_barrier
	s_setprio 1
	s_waitcnt lgkmcnt(6)
	v_mfma_scale_f32_16x16x128_f8f6f4 v[140:143], v[116:123], v[180:187], v[140:143], v153, v153 op_sel_hi:[0,0,0]
	v_mfma_scale_f32_16x16x128_f8f6f4 v[132:135], v[156:163], v[180:187], v[132:135], v153, v153 op_sel_hi:[0,0,0]
	s_waitcnt lgkmcnt(4)
	v_mfma_scale_f32_16x16x128_f8f6f4 v[124:127], v[116:123], v[188:195], v[124:127], v153, v153 op_sel_hi:[0,0,0]
	v_mfma_scale_f32_16x16x128_f8f6f4 v[108:111], v[156:163], v[188:195], v[108:111], v153, v153 op_sel_hi:[0,0,0]
	s_waitcnt lgkmcnt(2)
	v_mfma_scale_f32_16x16x128_f8f6f4 v[144:147], v[116:123], v[196:203], v[96:99], v153, v153 op_sel_hi:[0,0,0]
	v_mfma_scale_f32_16x16x128_f8f6f4 v[212:215], v[156:163], v[196:203], v[88:91], v153, v153 op_sel_hi:[0,0,0]
	s_waitcnt lgkmcnt(0)
	v_mfma_scale_f32_16x16x128_f8f6f4 v[216:219], v[116:123], v[204:211], v[80:83], v153, v153 op_sel_hi:[0,0,0]
	v_mfma_scale_f32_16x16x128_f8f6f4 v[220:223], v[156:163], v[204:211], v[72:75], v153, v153 op_sel_hi:[0,0,0]
	s_setprio 0
	s_setprio 1
	v_mfma_scale_f32_16x16x128_f8f6f4 v[136:139], v[164:171], v[180:187], v[136:139], v153, v153 op_sel_hi:[0,0,0]
	v_mfma_scale_f32_16x16x128_f8f6f4 v[128:131], v[172:179], v[180:187], v[128:131], v153, v153 op_sel_hi:[0,0,0]
	v_mfma_scale_f32_16x16x128_f8f6f4 v[112:115], v[164:171], v[188:195], v[112:115], v153, v153 op_sel_hi:[0,0,0]
	v_mfma_scale_f32_16x16x128_f8f6f4 v[100:103], v[172:179], v[188:195], v[100:103], v153, v153 op_sel_hi:[0,0,0]
	v_mfma_scale_f32_16x16x128_f8f6f4 v[180:183], v[164:171], v[196:203], v[92:95], v153, v153 op_sel_hi:[0,0,0]
	v_mfma_scale_f32_16x16x128_f8f6f4 v[184:187], v[172:179], v[196:203], v[84:87], v153, v153 op_sel_hi:[0,0,0]
	v_mfma_scale_f32_16x16x128_f8f6f4 v[188:191], v[164:171], v[204:211], v[76:79], v153, v153 op_sel_hi:[0,0,0]
	v_mfma_scale_f32_16x16x128_f8f6f4 v[192:195], v[172:179], v[204:211], v[68:71], v153, v153 op_sel_hi:[0,0,0]
	s_setprio 0
	s_barrier
	s_nop 4
	ds_read_b128 v[68:71], v152 offset:16384
	ds_read_b128 v[72:75], v152 offset:17408
	ds_read_b128 v[76:79], v152 offset:18432
	ds_read_b128 v[80:83], v152 offset:19456
	ds_read_b128 v[84:87], v152 offset:20480
	ds_read_b128 v[88:91], v152 offset:21504
	ds_read_b128 v[92:95], v152 offset:22528
	ds_read_b128 v[96:99], v152 offset:23552
	s_mov_b32 s72, m0
	s_mov_b32 m0, s3
	s_nop 2
	global_load_lds_dwordx4 v252, s[64:65]
	s_mov_b32 m0, s72
	s_nop 0
	s_mov_b32 s72, m0
	s_mov_b32 m0, s27
	s_nop 2
	global_load_lds_dwordx4 v253, s[64:65]
	s_mov_b32 m0, s72
	s_mov_b32 s64, m0
	s_mov_b32 m0, s33
	s_nop 2
	global_load_lds_dwordx4 v252, s[62:63]
	s_mov_b32 m0, s64
	s_nop 0
	s_mov_b32 s64, m0
	s_mov_b32 m0, s40
	s_nop 2
	global_load_lds_dwordx4 v253, s[62:63]
	s_mov_b32 m0, s64
	s_mov_b32 s62, m0
	s_mov_b32 m0, s2
	s_nop 2
	global_load_lds_dwordx4 v104, s[60:61]
	s_mov_b32 m0, s62
	s_nop 0
	s_mov_b32 s62, m0
	s_mov_b32 m0, s41
	s_nop 2
	global_load_lds_dwordx4 v105, s[60:61]
	s_mov_b32 m0, s62
	s_waitcnt vmcnt(8)
	s_waitcnt lgkmcnt(0)
	s_barrier
	s_cmp_lg_u32 s32, 0
	s_cbranch_scc1 .Lp7_rag_1
	s_setprio 1
	s_waitcnt lgkmcnt(6)
	v_mfma_scale_f32_16x16x128_f8f6f4 v[64:67], v[116:123], v[68:75], v[64:67], v153, v153 op_sel_hi:[0,0,0]
	v_mfma_scale_f32_16x16x128_f8f6f4 v[56:59], v[156:163], v[68:75], v[56:59], v153, v153 op_sel_hi:[0,0,0]
	s_waitcnt lgkmcnt(4)
	v_mfma_scale_f32_16x16x128_f8f6f4 v[48:51], v[116:123], v[76:83], v[48:51], v153, v153 op_sel_hi:[0,0,0]
	v_mfma_scale_f32_16x16x128_f8f6f4 v[204:207], v[156:163], v[76:83], v[40:43], v153, v153 op_sel_hi:[0,0,0]
	s_waitcnt lgkmcnt(2)
	v_mfma_scale_f32_16x16x128_f8f6f4 v[208:211], v[116:123], v[84:91], v[28:31], v153, v153 op_sel_hi:[0,0,0]
	v_mfma_scale_f32_16x16x128_f8f6f4 v[224:227], v[156:163], v[84:91], v[20:23], v153, v153 op_sel_hi:[0,0,0]
	s_waitcnt lgkmcnt(0)
	v_mfma_scale_f32_16x16x128_f8f6f4 v[228:231], v[116:123], v[92:99], v[12:15], v153, v153 op_sel_hi:[0,0,0]
	v_mfma_scale_f32_16x16x128_f8f6f4 v[232:235], v[156:163], v[92:99], v[4:7], v153, v153 op_sel_hi:[0,0,0]
	s_setprio 0
	s_setprio 1
	v_mfma_scale_f32_16x16x128_f8f6f4 v[60:63], v[164:171], v[68:75], v[60:63], v153, v153 op_sel_hi:[0,0,0]
	v_mfma_scale_f32_16x16x128_f8f6f4 v[52:55], v[172:179], v[68:75], v[52:55], v153, v153 op_sel_hi:[0,0,0]
	v_mfma_scale_f32_16x16x128_f8f6f4 v[32:35], v[172:179], v[76:83], v[32:35], v153, v153 op_sel_hi:[0,0,0]
	v_mfma_scale_f32_16x16x128_f8f6f4 v[236:239], v[164:171], v[76:83], v[44:47], v153, v153 op_sel_hi:[0,0,0]
	v_mfma_scale_f32_16x16x128_f8f6f4 v[240:243], v[164:171], v[84:91], v[24:27], v153, v153 op_sel_hi:[0,0,0]
	v_mfma_scale_f32_16x16x128_f8f6f4 v[244:247], v[172:179], v[84:91], v[16:19], v153, v153 op_sel_hi:[0,0,0]
	v_mfma_scale_f32_16x16x128_f8f6f4 v[248:251], v[164:171], v[92:99], v[8:11], v153, v153 op_sel_hi:[0,0,0]
	v_mfma_scale_f32_16x16x128_f8f6f4 v[148:151], v[172:179], v[92:99], v[0:3], v153, v153 op_sel_hi:[0,0,0]
	s_setprio 0
.Lp7_rag_1:
	s_barrier
	s_nop 3
	v_add_u32_e32 v8, 0x18000, v254
	ds_read_b128 v[0:3], v8
	ds_read_b128 v[4:7], v8 offset:1024
	ds_read_b128 v[116:119], v8 offset:2048
	ds_read_b128 v[120:123], v8 offset:3072
	v_add_u32_e32 v8, 0x1c000, v254
	ds_read_b128 v[156:159], v8
	ds_read_b128 v[160:163], v8 offset:1024
	ds_read_b128 v[164:167], v8 offset:2048
	ds_read_b128 v[168:171], v8 offset:3072
	ds_read_b128 v[8:11], v152 offset:32768
	ds_read_b128 v[12:15], v152 offset:33792
	ds_read_b128 v[16:19], v152 offset:34816
	ds_read_b128 v[20:23], v152 offset:35840
	ds_read_b128 v[24:27], v152 offset:36864
	ds_read_b128 v[28:31], v152 offset:37888
	ds_read_b128 v[40:43], v152 offset:38912
	ds_read_b128 v[44:47], v152 offset:39936
	s_mov_b32 s62, m0
	s_mov_b32 m0, s42
	s_nop 2
	global_load_lds_dwordx4 v106, s[60:61]
	s_mov_b32 m0, s62
	s_nop 0
	s_mov_b32 s62, m0
	s_mov_b32 m0, s43
	s_nop 2
	global_load_lds_dwordx4 v107, s[60:61]
	s_mov_b32 m0, s62
	s_waitcnt vmcnt(8)
	s_waitcnt lgkmcnt(0)
	s_barrier
	s_setprio 1
	s_waitcnt lgkmcnt(6)
	v_mfma_scale_f32_16x16x128_f8f6f4 v[140:143], v[0:7], v[8:15], v[140:143], v153, v153 op_sel_hi:[0,0,0]
	v_mfma_scale_f32_16x16x128_f8f6f4 v[132:135], v[116:123], v[8:15], v[132:135], v153, v153 op_sel_hi:[0,0,0]
	s_waitcnt lgkmcnt(4)
	v_mfma_scale_f32_16x16x128_f8f6f4 v[124:127], v[0:7], v[16:23], v[124:127], v153, v153 op_sel_hi:[0,0,0]
	v_mfma_scale_f32_16x16x128_f8f6f4 v[108:111], v[116:123], v[16:23], v[108:111], v153, v153 op_sel_hi:[0,0,0]
	s_waitcnt lgkmcnt(2)
	v_mfma_scale_f32_16x16x128_f8f6f4 v[96:99], v[0:7], v[24:31], v[144:147], v153, v153 op_sel_hi:[0,0,0]
	v_mfma_scale_f32_16x16x128_f8f6f4 v[88:91], v[116:123], v[24:31], v[212:215], v153, v153 op_sel_hi:[0,0,0]
	s_waitcnt lgkmcnt(0)
	v_mfma_scale_f32_16x16x128_f8f6f4 v[80:83], v[0:7], v[40:47], v[216:219], v153, v153 op_sel_hi:[0,0,0]
	v_mfma_scale_f32_16x16x128_f8f6f4 v[72:75], v[116:123], v[40:47], v[220:223], v153, v153 op_sel_hi:[0,0,0]
	s_setprio 0
	s_setprio 1
	v_mfma_scale_f32_16x16x128_f8f6f4 v[136:139], v[156:163], v[8:15], v[136:139], v153, v153 op_sel_hi:[0,0,0]
	v_mfma_scale_f32_16x16x128_f8f6f4 v[128:131], v[164:171], v[8:15], v[128:131], v153, v153 op_sel_hi:[0,0,0]
	v_mfma_scale_f32_16x16x128_f8f6f4 v[112:115], v[156:163], v[16:23], v[112:115], v153, v153 op_sel_hi:[0,0,0]
	v_mfma_scale_f32_16x16x128_f8f6f4 v[100:103], v[164:171], v[16:23], v[100:103], v153, v153 op_sel_hi:[0,0,0]
	v_mfma_scale_f32_16x16x128_f8f6f4 v[92:95], v[156:163], v[24:31], v[180:183], v153, v153 op_sel_hi:[0,0,0]
	v_mfma_scale_f32_16x16x128_f8f6f4 v[84:87], v[164:171], v[24:31], v[184:187], v153, v153 op_sel_hi:[0,0,0]
	v_mfma_scale_f32_16x16x128_f8f6f4 v[76:79], v[156:163], v[40:47], v[188:191], v153, v153 op_sel_hi:[0,0,0]
	v_mfma_scale_f32_16x16x128_f8f6f4 v[68:71], v[164:171], v[40:47], v[192:195], v153, v153 op_sel_hi:[0,0,0]
	s_setprio 0
	s_barrier
	ds_read_b128 v[172:175], v152 offset:49152
	ds_read_b128 v[176:179], v152 offset:50176
	ds_read_b128 v[180:183], v152 offset:51200
	ds_read_b128 v[184:187], v152 offset:52224
	ds_read_b128 v[188:191], v152 offset:53248
	ds_read_b128 v[192:195], v152 offset:54272
	ds_read_b128 v[196:199], v152 offset:55296
	ds_read_b128 v[200:203], v152 offset:56320
	s_mov_b32 s60, m0
	s_mov_b32 m0, s46
	s_nop 2
	global_load_lds_dwordx4 v252, s[56:57]
	s_mov_b32 m0, s60
	s_nop 0
	s_mov_b32 s60, m0
	s_mov_b32 m0, s48
	s_nop 2
	global_load_lds_dwordx4 v253, s[56:57]
	s_mov_b32 m0, s60
	s_mov_b32 s56, m0
	s_mov_b32 m0, s53
	s_nop 2
	global_load_lds_dwordx4 v252, s[58:59]
	s_mov_b32 m0, s56
	s_nop 0
	s_mov_b32 s56, m0
	s_mov_b32 m0, s54
	s_nop 2
	global_load_lds_dwordx4 v253, s[58:59]
	s_mov_b32 m0, s56
	s_nop 0
	s_mov_b32 s56, m0
	s_mov_b32 m0, s49
	s_nop 2
	global_load_lds_dwordx4 v104, s[36:37]
	s_mov_b32 m0, s56
	s_nop 0
	s_mov_b32 s56, m0
	s_mov_b32 m0, s52
	s_nop 2
	global_load_lds_dwordx4 v105, s[36:37]
	s_mov_b32 m0, s56
	s_waitcnt vmcnt(8)
	s_waitcnt lgkmcnt(0)
	s_barrier
	s_cmp_lg_u32 s32, 0
	s_cbranch_scc1 .Lp7_rag_3
	s_setprio 1
	s_waitcnt lgkmcnt(6)
	v_mfma_scale_f32_16x16x128_f8f6f4 v[64:67], v[0:7], v[172:179], v[64:67], v153, v153 op_sel_hi:[0,0,0]
	v_mfma_scale_f32_16x16x128_f8f6f4 v[56:59], v[116:123], v[172:179], v[56:59], v153, v153 op_sel_hi:[0,0,0]
	s_waitcnt lgkmcnt(4)
	v_mfma_scale_f32_16x16x128_f8f6f4 v[48:51], v[0:7], v[180:187], v[48:51], v153, v153 op_sel_hi:[0,0,0]
	v_mfma_scale_f32_16x16x128_f8f6f4 v[40:43], v[116:123], v[180:187], v[204:207], v153, v153 op_sel_hi:[0,0,0]
	s_waitcnt lgkmcnt(2)
	v_mfma_scale_f32_16x16x128_f8f6f4 v[28:31], v[0:7], v[188:195], v[208:211], v153, v153 op_sel_hi:[0,0,0]
	v_mfma_scale_f32_16x16x128_f8f6f4 v[20:23], v[116:123], v[188:195], v[224:227], v153, v153 op_sel_hi:[0,0,0]
	s_waitcnt lgkmcnt(0)
	v_mfma_scale_f32_16x16x128_f8f6f4 v[12:15], v[0:7], v[196:203], v[228:231], v153, v153 op_sel_hi:[0,0,0]
	v_mfma_scale_f32_16x16x128_f8f6f4 v[4:7], v[116:123], v[196:203], v[232:235], v153, v153 op_sel_hi:[0,0,0]
	s_setprio 0
	s_setprio 1
	v_mfma_scale_f32_16x16x128_f8f6f4 v[60:63], v[156:163], v[172:179], v[60:63], v153, v153 op_sel_hi:[0,0,0]
	v_mfma_scale_f32_16x16x128_f8f6f4 v[52:55], v[164:171], v[172:179], v[52:55], v153, v153 op_sel_hi:[0,0,0]
	v_mfma_scale_f32_16x16x128_f8f6f4 v[44:47], v[156:163], v[180:187], v[236:239], v153, v153 op_sel_hi:[0,0,0]
	v_mfma_scale_f32_16x16x128_f8f6f4 v[32:35], v[164:171], v[180:187], v[32:35], v153, v153 op_sel_hi:[0,0,0]
	v_mfma_scale_f32_16x16x128_f8f6f4 v[24:27], v[156:163], v[188:195], v[240:243], v153, v153 op_sel_hi:[0,0,0]
	v_mfma_scale_f32_16x16x128_f8f6f4 v[16:19], v[164:171], v[188:195], v[244:247], v153, v153 op_sel_hi:[0,0,0]
	v_mfma_scale_f32_16x16x128_f8f6f4 v[8:11], v[156:163], v[196:203], v[248:251], v153, v153 op_sel_hi:[0,0,0]
	v_mfma_scale_f32_16x16x128_f8f6f4 v[0:3], v[164:171], v[196:203], v[148:151], v153, v153 op_sel_hi:[0,0,0]
	s_setprio 0
.Lp7_rag_3:
	s_barrier
	s_add_i32 s83, s83, 2
	s_add_u32 s19, s19, 0x100
	s_addc_u32 s25, s25, 0
	s_add_u32 s81, s81, 0x100
	s_addc_u32 s82, s82, 0
	s_cmp_gt_u32 s83, 13
	s_mov_b64 s[36:37], s[50:51]
	s_cbranch_scc1 .LBB0_1039

.LBB0_1041:
	v_mbcnt_lo_u32_b32 v146, -1, 0
	v_mbcnt_hi_u32_b32 v146, -1, v146
	s_lshl_b32 s19, s26, 7
	v_ashrrev_i32_e32 v36, 1, v146
	s_ashr_i32 s25, s24, 31
	v_and_b32_e32 v36, -8, v36
	s_or_b32 s19, s19, s45
	s_lshl_b64 s[24:25], s[24:25], 14
	v_add_u32_e32 v144, s19, v36
	s_add_u32 s24, s68, s24
	s_addc_u32 s25, s69, s25
	v_ashrrev_i32_e32 v145, 31, v144
	v_lshl_add_u64 v[104:105], v[144:145], 2, s[24:25]
	global_load_dwordx4 v[120:123], v[104:105], off
	global_load_dwordx4 v[36:39], v[104:105], off offset:16
	s_movk_i32 s19, 0x2000
	v_add_co_u32_e32 v106, vcc, s19, v104
	s_mov_b64 s[24:25], 0x2000
	s_nop 0
	v_addc_co_u32_e32 v107, vcc, 0, v105, vcc
	v_lshl_add_u64 v[104:105], v[104:105], 0, s[24:25]
	global_load_dwordx4 v[116:119], v[106:107], off
	v_and_or_b32 v146, v146, 15, s44
	global_load_dwordx4 v[104:107], v[104:105], off offset:16
	v_lshl_add_u32 v146, s80, 8, v146
	s_mov_b32 s19, 0x40000
	v_lshl_add_u32 v146, v146, 11, v144
	s_mov_b32 s24, 0x3b000000
	v_mov_b32_e32 v144, 0xc01d265f
	v_mov_b32_e32 v156, 1.0
	s_waitcnt vmcnt(0)
	v_pk_fma_f32 v[140:141], v[140:141], s[24:25], v[120:121] op_sel_hi:[1,0,1]
	v_pk_fma_f32 v[142:143], v[142:143], s[24:25], v[122:123] op_sel_hi:[1,0,1]
	v_pk_fma_f32 v[136:137], v[136:137], s[24:25], v[116:117] op_sel_hi:[1,0,1]
	v_pk_fma_f32 v[138:139], v[138:139], s[24:25], v[118:119] op_sel_hi:[1,0,1]
	v_min_f32_e32 v140, 0x40e00000, v140
	v_min_f32_e32 v141, 0x40e00000, v141
	v_min_f32_e32 v142, 0x40e00000, v142
	v_min_f32_e32 v143, 0x40e00000, v143
	v_pk_mul_f32 v[148:149], v[140:141], v[144:145] op_sel_hi:[1,0]
	v_pk_mul_f32 v[150:151], v[142:143], v[144:145] op_sel_hi:[1,0]
	v_exp_f32_e32 v148, v148
	v_exp_f32_e32 v149, v149
	v_exp_f32_e32 v150, v150
	v_exp_f32_e32 v151, v151
	v_med3_f32 v136, v136, s75, v154
	v_med3_f32 v137, v137, s75, v154
	v_med3_f32 v138, v138, s75, v154
	v_med3_f32 v139, v139, s75, v154
	v_pk_add_f32 v[148:149], v[148:149], v[156:157] op_sel_hi:[1,0]
	v_pk_add_f32 v[150:151], v[150:151], v[156:157] op_sel_hi:[1,0]
	v_rcp_f32_e32 v148, v148
	v_rcp_f32_e32 v149, v149
	v_rcp_f32_e32 v150, v150
	v_rcp_f32_e32 v151, v151
	v_pk_add_f32 v[136:137], v[136:137], v[156:157] op_sel_hi:[1,0]
	v_pk_add_f32 v[138:139], v[138:139], v[156:157] op_sel_hi:[1,0]
	v_pk_mul_f32 v[140:141], v[140:141], v[148:149]
	v_pk_mul_f32 v[142:143], v[142:143], v[150:151]
	v_pk_mul_f32 v[136:137], v[136:137], v[140:141]
	v_pk_mul_f32 v[138:139], v[138:139], v[142:143]
	v_pk_fma_f32 v[132:133], v[132:133], s[24:25], v[36:37] op_sel_hi:[1,0,1]
	v_pk_fma_f32 v[134:135], v[134:135], s[24:25], v[38:39] op_sel_hi:[1,0,1]
	v_pk_fma_f32 v[128:129], v[128:129], s[24:25], v[104:105] op_sel_hi:[1,0,1]
	v_pk_fma_f32 v[130:131], v[130:131], s[24:25], v[106:107] op_sel_hi:[1,0,1]
	v_min_f32_e32 v132, 0x40e00000, v132
	v_min_f32_e32 v133, 0x40e00000, v133
	v_min_f32_e32 v134, 0x40e00000, v134
	v_min_f32_e32 v135, 0x40e00000, v135
	v_pk_mul_f32 v[148:149], v[132:133], v[144:145] op_sel_hi:[1,0]
	v_pk_mul_f32 v[150:151], v[134:135], v[144:145] op_sel_hi:[1,0]
	v_exp_f32_e32 v148, v148
	v_exp_f32_e32 v149, v149
	v_exp_f32_e32 v150, v150
	v_exp_f32_e32 v151, v151
	v_med3_f32 v128, v128, s75, v154
	v_med3_f32 v129, v129, s75, v154
	v_med3_f32 v130, v130, s75, v154
	v_med3_f32 v131, v131, s75, v154
	v_pk_add_f32 v[148:149], v[148:149], v[156:157] op_sel_hi:[1,0]
	v_pk_add_f32 v[150:151], v[150:151], v[156:157] op_sel_hi:[1,0]
	v_rcp_f32_e32 v148, v148
	v_rcp_f32_e32 v149, v149
	v_rcp_f32_e32 v150, v150
	v_rcp_f32_e32 v151, v151
	v_pk_add_f32 v[128:129], v[128:129], v[156:157] op_sel_hi:[1,0]
	v_pk_add_f32 v[130:131], v[130:131], v[156:157] op_sel_hi:[1,0]
	v_pk_mul_f32 v[132:133], v[132:133], v[148:149]
	v_pk_mul_f32 v[134:135], v[134:135], v[150:151]
	v_pk_mul_f32 v[128:129], v[128:129], v[132:133]
	v_pk_mul_f32 v[130:131], v[130:131], v[134:135]
	v_cvt_pk_fp8_f32 v140, v136, v137
	v_cvt_pk_fp8_f32 v140, v138, v139 op_sel:[0,0,1]
	v_cvt_pk_fp8_f32 v141, v128, v129
	v_cvt_pk_fp8_f32 v141, v130, v131 op_sel:[0,0,1]
	global_store_dwordx2 v146, v[140:141], s[14:15]
	v_pk_fma_f32 v[124:125], v[124:125], s[24:25], v[120:121] op_sel_hi:[1,0,1]
	v_pk_fma_f32 v[126:127], v[126:127], s[24:25], v[122:123] op_sel_hi:[1,0,1]
	v_pk_fma_f32 v[112:113], v[112:113], s[24:25], v[116:117] op_sel_hi:[1,0,1]
	v_pk_fma_f32 v[114:115], v[114:115], s[24:25], v[118:119] op_sel_hi:[1,0,1]
	v_min_f32_e32 v124, 0x40e00000, v124
	v_min_f32_e32 v125, 0x40e00000, v125
	v_min_f32_e32 v126, 0x40e00000, v126
	v_min_f32_e32 v127, 0x40e00000, v127
	v_pk_mul_f32 v[148:149], v[124:125], v[144:145] op_sel_hi:[1,0]
	v_pk_mul_f32 v[150:151], v[126:127], v[144:145] op_sel_hi:[1,0]
	v_exp_f32_e32 v148, v148
	v_exp_f32_e32 v149, v149
	v_exp_f32_e32 v150, v150
	v_exp_f32_e32 v151, v151
	v_med3_f32 v112, v112, s75, v154
	v_med3_f32 v113, v113, s75, v154
	v_med3_f32 v114, v114, s75, v154
	v_med3_f32 v115, v115, s75, v154
	v_pk_add_f32 v[148:149], v[148:149], v[156:157] op_sel_hi:[1,0]
	v_pk_add_f32 v[150:151], v[150:151], v[156:157] op_sel_hi:[1,0]
	v_rcp_f32_e32 v148, v148
	v_rcp_f32_e32 v149, v149
	v_rcp_f32_e32 v150, v150
	v_rcp_f32_e32 v151, v151
	v_pk_add_f32 v[112:113], v[112:113], v[156:157] op_sel_hi:[1,0]
	v_pk_add_f32 v[114:115], v[114:115], v[156:157] op_sel_hi:[1,0]
	v_pk_mul_f32 v[124:125], v[124:125], v[148:149]
	v_pk_mul_f32 v[126:127], v[126:127], v[150:151]
	v_pk_mul_f32 v[112:113], v[112:113], v[124:125]
	v_pk_mul_f32 v[114:115], v[114:115], v[126:127]
	v_pk_fma_f32 v[108:109], v[108:109], s[24:25], v[36:37] op_sel_hi:[1,0,1]
	v_pk_fma_f32 v[110:111], v[110:111], s[24:25], v[38:39] op_sel_hi:[1,0,1]
	v_pk_fma_f32 v[100:101], v[100:101], s[24:25], v[104:105] op_sel_hi:[1,0,1]
	v_pk_fma_f32 v[102:103], v[102:103], s[24:25], v[106:107] op_sel_hi:[1,0,1]
	v_min_f32_e32 v108, 0x40e00000, v108
	v_min_f32_e32 v109, 0x40e00000, v109
	v_min_f32_e32 v110, 0x40e00000, v110
	v_min_f32_e32 v111, 0x40e00000, v111
	v_pk_mul_f32 v[148:149], v[108:109], v[144:145] op_sel_hi:[1,0]
	v_pk_mul_f32 v[150:151], v[110:111], v[144:145] op_sel_hi:[1,0]
	v_exp_f32_e32 v148, v148
	v_exp_f32_e32 v149, v149
	v_exp_f32_e32 v150, v150
	v_exp_f32_e32 v151, v151
	v_med3_f32 v100, v100, s75, v154
	v_med3_f32 v101, v101, s75, v154
	v_med3_f32 v102, v102, s75, v154
	v_med3_f32 v103, v103, s75, v154
	v_pk_add_f32 v[148:149], v[148:149], v[156:157] op_sel_hi:[1,0]
	v_pk_add_f32 v[150:151], v[150:151], v[156:157] op_sel_hi:[1,0]
	v_rcp_f32_e32 v148, v148
	v_rcp_f32_e32 v149, v149
	v_rcp_f32_e32 v150, v150
	v_rcp_f32_e32 v151, v151
	v_pk_add_f32 v[100:101], v[100:101], v[156:157] op_sel_hi:[1,0]
	v_pk_add_f32 v[102:103], v[102:103], v[156:157] op_sel_hi:[1,0]
	v_pk_mul_f32 v[108:109], v[108:109], v[148:149]
	v_pk_mul_f32 v[110:111], v[110:111], v[150:151]
	v_pk_mul_f32 v[100:101], v[100:101], v[108:109]
	v_pk_mul_f32 v[102:103], v[102:103], v[110:111]
	v_cvt_pk_fp8_f32 v124, v112, v113
	v_cvt_pk_fp8_f32 v124, v114, v115 op_sel:[0,0,1]
	v_cvt_pk_fp8_f32 v125, v100, v101
	v_cvt_pk_fp8_f32 v125, v102, v103 op_sel:[0,0,1]
	s_add_u32 vcc_lo, s14, 0x8000
	s_addc_u32 vcc_hi, s15, 0
	global_store_dwordx2 v146, v[124:125], vcc
	v_pk_fma_f32 v[96:97], v[96:97], s[24:25], v[120:121] op_sel_hi:[1,0,1]
	v_pk_fma_f32 v[98:99], v[98:99], s[24:25], v[122:123] op_sel_hi:[1,0,1]
	v_pk_fma_f32 v[92:93], v[92:93], s[24:25], v[116:117] op_sel_hi:[1,0,1]
	v_pk_fma_f32 v[94:95], v[94:95], s[24:25], v[118:119] op_sel_hi:[1,0,1]
	v_min_f32_e32 v96, 0x40e00000, v96
	v_min_f32_e32 v97, 0x40e00000, v97
	v_min_f32_e32 v98, 0x40e00000, v98
	v_min_f32_e32 v99, 0x40e00000, v99
	v_pk_mul_f32 v[148:149], v[96:97], v[144:145] op_sel_hi:[1,0]
	v_pk_mul_f32 v[150:151], v[98:99], v[144:145] op_sel_hi:[1,0]
	v_exp_f32_e32 v148, v148
	v_exp_f32_e32 v149, v149
	v_exp_f32_e32 v150, v150
	v_exp_f32_e32 v151, v151
	v_med3_f32 v92, v92, s75, v154
	v_med3_f32 v93, v93, s75, v154
	v_med3_f32 v94, v94, s75, v154
	v_med3_f32 v95, v95, s75, v154
	v_pk_add_f32 v[148:149], v[148:149], v[156:157] op_sel_hi:[1,0]
	v_pk_add_f32 v[150:151], v[150:151], v[156:157] op_sel_hi:[1,0]
	v_rcp_f32_e32 v148, v148
	v_rcp_f32_e32 v149, v149
	v_rcp_f32_e32 v150, v150
	v_rcp_f32_e32 v151, v151
	v_pk_add_f32 v[92:93], v[92:93], v[156:157] op_sel_hi:[1,0]
	v_pk_add_f32 v[94:95], v[94:95], v[156:157] op_sel_hi:[1,0]
	v_pk_mul_f32 v[96:97], v[96:97], v[148:149]
	v_pk_mul_f32 v[98:99], v[98:99], v[150:151]
	v_pk_mul_f32 v[92:93], v[92:93], v[96:97]
	v_pk_mul_f32 v[94:95], v[94:95], v[98:99]
	v_pk_fma_f32 v[88:89], v[88:89], s[24:25], v[36:37] op_sel_hi:[1,0,1]
	v_pk_fma_f32 v[90:91], v[90:91], s[24:25], v[38:39] op_sel_hi:[1,0,1]
	v_pk_fma_f32 v[84:85], v[84:85], s[24:25], v[104:105] op_sel_hi:[1,0,1]
	v_pk_fma_f32 v[86:87], v[86:87], s[24:25], v[106:107] op_sel_hi:[1,0,1]
	v_min_f32_e32 v88, 0x40e00000, v88
	v_min_f32_e32 v89, 0x40e00000, v89
	v_min_f32_e32 v90, 0x40e00000, v90
	v_min_f32_e32 v91, 0x40e00000, v91
	v_pk_mul_f32 v[148:149], v[88:89], v[144:145] op_sel_hi:[1,0]
	v_pk_mul_f32 v[150:151], v[90:91], v[144:145] op_sel_hi:[1,0]
	v_exp_f32_e32 v148, v148
	v_exp_f32_e32 v149, v149
	v_exp_f32_e32 v150, v150
	v_exp_f32_e32 v151, v151
	v_med3_f32 v84, v84, s75, v154
	v_med3_f32 v85, v85, s75, v154
	v_med3_f32 v86, v86, s75, v154
	v_med3_f32 v87, v87, s75, v154
	v_pk_add_f32 v[148:149], v[148:149], v[156:157] op_sel_hi:[1,0]
	v_pk_add_f32 v[150:151], v[150:151], v[156:157] op_sel_hi:[1,0]
	v_rcp_f32_e32 v148, v148
	v_rcp_f32_e32 v149, v149
	v_rcp_f32_e32 v150, v150
	v_rcp_f32_e32 v151, v151
	v_pk_add_f32 v[84:85], v[84:85], v[156:157] op_sel_hi:[1,0]
	v_pk_add_f32 v[86:87], v[86:87], v[156:157] op_sel_hi:[1,0]
	v_pk_mul_f32 v[88:89], v[88:89], v[148:149]
	v_pk_mul_f32 v[90:91], v[90:91], v[150:151]
	v_pk_mul_f32 v[84:85], v[84:85], v[88:89]
	v_pk_mul_f32 v[86:87], v[86:87], v[90:91]
	v_cvt_pk_fp8_f32 v96, v92, v93
	v_cvt_pk_fp8_f32 v96, v94, v95 op_sel:[0,0,1]
	v_cvt_pk_fp8_f32 v97, v84, v85
	v_cvt_pk_fp8_f32 v97, v86, v87 op_sel:[0,0,1]
	s_add_u32 vcc_lo, s14, 0x10000
	s_addc_u32 vcc_hi, s15, 0
	global_store_dwordx2 v146, v[96:97], vcc
	v_pk_fma_f32 v[80:81], v[80:81], s[24:25], v[120:121] op_sel_hi:[1,0,1]
	v_pk_fma_f32 v[82:83], v[82:83], s[24:25], v[122:123] op_sel_hi:[1,0,1]
	v_pk_fma_f32 v[76:77], v[76:77], s[24:25], v[116:117] op_sel_hi:[1,0,1]
	v_pk_fma_f32 v[78:79], v[78:79], s[24:25], v[118:119] op_sel_hi:[1,0,1]
	v_min_f32_e32 v80, 0x40e00000, v80
	v_min_f32_e32 v81, 0x40e00000, v81
	v_min_f32_e32 v82, 0x40e00000, v82
	v_min_f32_e32 v83, 0x40e00000, v83
	v_pk_mul_f32 v[148:149], v[80:81], v[144:145] op_sel_hi:[1,0]
	v_pk_mul_f32 v[150:151], v[82:83], v[144:145] op_sel_hi:[1,0]
	v_exp_f32_e32 v148, v148
	v_exp_f32_e32 v149, v149
	v_exp_f32_e32 v150, v150
	v_exp_f32_e32 v151, v151
	v_med3_f32 v76, v76, s75, v154
	v_med3_f32 v77, v77, s75, v154
	v_med3_f32 v78, v78, s75, v154
	v_med3_f32 v79, v79, s75, v154
	v_pk_add_f32 v[148:149], v[148:149], v[156:157] op_sel_hi:[1,0]
	v_pk_add_f32 v[150:151], v[150:151], v[156:157] op_sel_hi:[1,0]
	v_rcp_f32_e32 v148, v148
	v_rcp_f32_e32 v149, v149
	v_rcp_f32_e32 v150, v150
	v_rcp_f32_e32 v151, v151
	v_pk_add_f32 v[76:77], v[76:77], v[156:157] op_sel_hi:[1,0]
	v_pk_add_f32 v[78:79], v[78:79], v[156:157] op_sel_hi:[1,0]
	v_pk_mul_f32 v[80:81], v[80:81], v[148:149]
	v_pk_mul_f32 v[82:83], v[82:83], v[150:151]
	v_pk_mul_f32 v[76:77], v[76:77], v[80:81]
	v_pk_mul_f32 v[78:79], v[78:79], v[82:83]
	v_pk_fma_f32 v[72:73], v[72:73], s[24:25], v[36:37] op_sel_hi:[1,0,1]
	v_pk_fma_f32 v[74:75], v[74:75], s[24:25], v[38:39] op_sel_hi:[1,0,1]
	v_pk_fma_f32 v[68:69], v[68:69], s[24:25], v[104:105] op_sel_hi:[1,0,1]
	v_pk_fma_f32 v[70:71], v[70:71], s[24:25], v[106:107] op_sel_hi:[1,0,1]
	v_min_f32_e32 v72, 0x40e00000, v72
	v_min_f32_e32 v73, 0x40e00000, v73
	v_min_f32_e32 v74, 0x40e00000, v74
	v_min_f32_e32 v75, 0x40e00000, v75
	v_pk_mul_f32 v[148:149], v[72:73], v[144:145] op_sel_hi:[1,0]
	v_pk_mul_f32 v[150:151], v[74:75], v[144:145] op_sel_hi:[1,0]
	v_exp_f32_e32 v148, v148
	v_exp_f32_e32 v149, v149
	v_exp_f32_e32 v150, v150
	v_exp_f32_e32 v151, v151
	v_med3_f32 v68, v68, s75, v154
	v_med3_f32 v69, v69, s75, v154
	v_med3_f32 v70, v70, s75, v154
	v_med3_f32 v71, v71, s75, v154
	v_pk_add_f32 v[148:149], v[148:149], v[156:157] op_sel_hi:[1,0]
	v_pk_add_f32 v[150:151], v[150:151], v[156:157] op_sel_hi:[1,0]
	v_rcp_f32_e32 v148, v148
	v_rcp_f32_e32 v149, v149
	v_rcp_f32_e32 v150, v150
	v_rcp_f32_e32 v151, v151
	v_pk_add_f32 v[68:69], v[68:69], v[156:157] op_sel_hi:[1,0]
	v_pk_add_f32 v[70:71], v[70:71], v[156:157] op_sel_hi:[1,0]
	v_pk_mul_f32 v[72:73], v[72:73], v[148:149]
	v_pk_mul_f32 v[74:75], v[74:75], v[150:151]
	v_pk_mul_f32 v[68:69], v[68:69], v[72:73]
	v_pk_mul_f32 v[70:71], v[70:71], v[74:75]
	v_cvt_pk_fp8_f32 v80, v76, v77
	v_cvt_pk_fp8_f32 v80, v78, v79 op_sel:[0,0,1]
	v_cvt_pk_fp8_f32 v81, v68, v69
	v_cvt_pk_fp8_f32 v81, v70, v71 op_sel:[0,0,1]
	s_add_u32 vcc_lo, s14, 0x18000
	s_addc_u32 vcc_hi, s15, 0
	global_store_dwordx2 v146, v[80:81], vcc
	v_pk_fma_f32 v[64:65], v[64:65], s[24:25], v[120:121] op_sel_hi:[1,0,1]
	v_pk_fma_f32 v[66:67], v[66:67], s[24:25], v[122:123] op_sel_hi:[1,0,1]
	v_pk_fma_f32 v[60:61], v[60:61], s[24:25], v[116:117] op_sel_hi:[1,0,1]
	v_pk_fma_f32 v[62:63], v[62:63], s[24:25], v[118:119] op_sel_hi:[1,0,1]
	v_min_f32_e32 v64, 0x40e00000, v64
	v_min_f32_e32 v65, 0x40e00000, v65
	v_min_f32_e32 v66, 0x40e00000, v66
	v_min_f32_e32 v67, 0x40e00000, v67
	v_pk_mul_f32 v[148:149], v[64:65], v[144:145] op_sel_hi:[1,0]
	v_pk_mul_f32 v[150:151], v[66:67], v[144:145] op_sel_hi:[1,0]
	v_exp_f32_e32 v148, v148
	v_exp_f32_e32 v149, v149
	v_exp_f32_e32 v150, v150
	v_exp_f32_e32 v151, v151
	v_med3_f32 v60, v60, s75, v154
	v_med3_f32 v61, v61, s75, v154
	v_med3_f32 v62, v62, s75, v154
	v_med3_f32 v63, v63, s75, v154
	v_pk_add_f32 v[148:149], v[148:149], v[156:157] op_sel_hi:[1,0]
	v_pk_add_f32 v[150:151], v[150:151], v[156:157] op_sel_hi:[1,0]
	v_rcp_f32_e32 v148, v148
	v_rcp_f32_e32 v149, v149
	v_rcp_f32_e32 v150, v150
	v_rcp_f32_e32 v151, v151
	v_pk_add_f32 v[60:61], v[60:61], v[156:157] op_sel_hi:[1,0]
	v_pk_add_f32 v[62:63], v[62:63], v[156:157] op_sel_hi:[1,0]
	v_pk_mul_f32 v[64:65], v[64:65], v[148:149]
	v_pk_mul_f32 v[66:67], v[66:67], v[150:151]
	v_pk_mul_f32 v[60:61], v[60:61], v[64:65]
	v_pk_mul_f32 v[62:63], v[62:63], v[66:67]
	v_pk_fma_f32 v[56:57], v[56:57], s[24:25], v[36:37] op_sel_hi:[1,0,1]
	v_pk_fma_f32 v[58:59], v[58:59], s[24:25], v[38:39] op_sel_hi:[1,0,1]
	v_pk_fma_f32 v[52:53], v[52:53], s[24:25], v[104:105] op_sel_hi:[1,0,1]
	v_pk_fma_f32 v[54:55], v[54:55], s[24:25], v[106:107] op_sel_hi:[1,0,1]
	v_min_f32_e32 v56, 0x40e00000, v56
	v_min_f32_e32 v57, 0x40e00000, v57
	v_min_f32_e32 v58, 0x40e00000, v58
	v_min_f32_e32 v59, 0x40e00000, v59
	v_pk_mul_f32 v[148:149], v[56:57], v[144:145] op_sel_hi:[1,0]
	v_pk_mul_f32 v[150:151], v[58:59], v[144:145] op_sel_hi:[1,0]
	v_exp_f32_e32 v148, v148
	v_exp_f32_e32 v149, v149
	v_exp_f32_e32 v150, v150
	v_exp_f32_e32 v151, v151
	v_med3_f32 v52, v52, s75, v154
	v_med3_f32 v53, v53, s75, v154
	v_med3_f32 v54, v54, s75, v154
	v_med3_f32 v55, v55, s75, v154
	v_pk_add_f32 v[148:149], v[148:149], v[156:157] op_sel_hi:[1,0]
	v_pk_add_f32 v[150:151], v[150:151], v[156:157] op_sel_hi:[1,0]
	v_rcp_f32_e32 v148, v148
	v_rcp_f32_e32 v149, v149
	v_rcp_f32_e32 v150, v150
	v_rcp_f32_e32 v151, v151
	v_pk_add_f32 v[52:53], v[52:53], v[156:157] op_sel_hi:[1,0]
	v_pk_add_f32 v[54:55], v[54:55], v[156:157] op_sel_hi:[1,0]
	v_pk_mul_f32 v[56:57], v[56:57], v[148:149]
	v_pk_mul_f32 v[58:59], v[58:59], v[150:151]
	v_pk_mul_f32 v[52:53], v[52:53], v[56:57]
	v_pk_mul_f32 v[54:55], v[54:55], v[58:59]
	v_cvt_pk_fp8_f32 v64, v60, v61
	v_cvt_pk_fp8_f32 v64, v62, v63 op_sel:[0,0,1]
	v_cvt_pk_fp8_f32 v65, v52, v53
	v_cvt_pk_fp8_f32 v65, v54, v55 op_sel:[0,0,1]
	s_add_u32 vcc_lo, s14, 0x40000
	s_addc_u32 vcc_hi, s15, 0
	global_store_dwordx2 v146, v[64:65], vcc
	v_pk_fma_f32 v[48:49], v[48:49], s[24:25], v[120:121] op_sel_hi:[1,0,1]
	v_pk_fma_f32 v[50:51], v[50:51], s[24:25], v[122:123] op_sel_hi:[1,0,1]
	v_pk_fma_f32 v[44:45], v[44:45], s[24:25], v[116:117] op_sel_hi:[1,0,1]
	v_pk_fma_f32 v[46:47], v[46:47], s[24:25], v[118:119] op_sel_hi:[1,0,1]
	v_min_f32_e32 v48, 0x40e00000, v48
	v_min_f32_e32 v49, 0x40e00000, v49
	v_min_f32_e32 v50, 0x40e00000, v50
	v_min_f32_e32 v51, 0x40e00000, v51
	v_pk_mul_f32 v[148:149], v[48:49], v[144:145] op_sel_hi:[1,0]
	v_pk_mul_f32 v[150:151], v[50:51], v[144:145] op_sel_hi:[1,0]
	v_exp_f32_e32 v148, v148
	v_exp_f32_e32 v149, v149
	v_exp_f32_e32 v150, v150
	v_exp_f32_e32 v151, v151
	v_med3_f32 v44, v44, s75, v154
	v_med3_f32 v45, v45, s75, v154
	v_med3_f32 v46, v46, s75, v154
	v_med3_f32 v47, v47, s75, v154
	v_pk_add_f32 v[148:149], v[148:149], v[156:157] op_sel_hi:[1,0]
	v_pk_add_f32 v[150:151], v[150:151], v[156:157] op_sel_hi:[1,0]
	v_rcp_f32_e32 v148, v148
	v_rcp_f32_e32 v149, v149
	v_rcp_f32_e32 v150, v150
	v_rcp_f32_e32 v151, v151
	v_pk_add_f32 v[44:45], v[44:45], v[156:157] op_sel_hi:[1,0]
	v_pk_add_f32 v[46:47], v[46:47], v[156:157] op_sel_hi:[1,0]
	v_pk_mul_f32 v[48:49], v[48:49], v[148:149]
	v_pk_mul_f32 v[50:51], v[50:51], v[150:151]
	v_pk_mul_f32 v[44:45], v[44:45], v[48:49]
	v_pk_mul_f32 v[46:47], v[46:47], v[50:51]
	v_pk_fma_f32 v[40:41], v[40:41], s[24:25], v[36:37] op_sel_hi:[1,0,1]
	v_pk_fma_f32 v[42:43], v[42:43], s[24:25], v[38:39] op_sel_hi:[1,0,1]
	v_pk_fma_f32 v[32:33], v[32:33], s[24:25], v[104:105] op_sel_hi:[1,0,1]
	v_pk_fma_f32 v[34:35], v[34:35], s[24:25], v[106:107] op_sel_hi:[1,0,1]
	v_min_f32_e32 v40, 0x40e00000, v40
	v_min_f32_e32 v41, 0x40e00000, v41
	v_min_f32_e32 v42, 0x40e00000, v42
	v_min_f32_e32 v43, 0x40e00000, v43
	v_pk_mul_f32 v[148:149], v[40:41], v[144:145] op_sel_hi:[1,0]
	v_pk_mul_f32 v[150:151], v[42:43], v[144:145] op_sel_hi:[1,0]
	v_exp_f32_e32 v148, v148
	v_exp_f32_e32 v149, v149
	v_exp_f32_e32 v150, v150
	v_exp_f32_e32 v151, v151
	v_med3_f32 v32, v32, s75, v154
	v_med3_f32 v33, v33, s75, v154
	v_med3_f32 v34, v34, s75, v154
	v_med3_f32 v35, v35, s75, v154
	v_pk_add_f32 v[148:149], v[148:149], v[156:157] op_sel_hi:[1,0]
	v_pk_add_f32 v[150:151], v[150:151], v[156:157] op_sel_hi:[1,0]
	v_rcp_f32_e32 v148, v148
	v_rcp_f32_e32 v149, v149
	v_rcp_f32_e32 v150, v150
	v_rcp_f32_e32 v151, v151
	v_pk_add_f32 v[32:33], v[32:33], v[156:157] op_sel_hi:[1,0]
	v_pk_add_f32 v[34:35], v[34:35], v[156:157] op_sel_hi:[1,0]
	v_pk_mul_f32 v[40:41], v[40:41], v[148:149]
	v_pk_mul_f32 v[42:43], v[42:43], v[150:151]
	v_pk_mul_f32 v[32:33], v[32:33], v[40:41]
	v_pk_mul_f32 v[34:35], v[34:35], v[42:43]
	v_cvt_pk_fp8_f32 v48, v44, v45
	v_cvt_pk_fp8_f32 v48, v46, v47 op_sel:[0,0,1]
	v_cvt_pk_fp8_f32 v49, v32, v33
	v_cvt_pk_fp8_f32 v49, v34, v35 op_sel:[0,0,1]
	s_add_u32 vcc_lo, s14, 0x48000
	s_addc_u32 vcc_hi, s15, 0
	global_store_dwordx2 v146, v[48:49], vcc
	v_pk_fma_f32 v[28:29], v[28:29], s[24:25], v[120:121] op_sel_hi:[1,0,1]
	v_pk_fma_f32 v[30:31], v[30:31], s[24:25], v[122:123] op_sel_hi:[1,0,1]
	v_pk_fma_f32 v[24:25], v[24:25], s[24:25], v[116:117] op_sel_hi:[1,0,1]
	v_pk_fma_f32 v[26:27], v[26:27], s[24:25], v[118:119] op_sel_hi:[1,0,1]
	v_min_f32_e32 v28, 0x40e00000, v28
	v_min_f32_e32 v29, 0x40e00000, v29
	v_min_f32_e32 v30, 0x40e00000, v30
	v_min_f32_e32 v31, 0x40e00000, v31
	v_pk_mul_f32 v[148:149], v[28:29], v[144:145] op_sel_hi:[1,0]
	v_pk_mul_f32 v[150:151], v[30:31], v[144:145] op_sel_hi:[1,0]
	v_exp_f32_e32 v148, v148
	v_exp_f32_e32 v149, v149
	v_exp_f32_e32 v150, v150
	v_exp_f32_e32 v151, v151
	v_med3_f32 v24, v24, s75, v154
	v_med3_f32 v25, v25, s75, v154
	v_med3_f32 v26, v26, s75, v154
	v_med3_f32 v27, v27, s75, v154
	v_pk_add_f32 v[148:149], v[148:149], v[156:157] op_sel_hi:[1,0]
	v_pk_add_f32 v[150:151], v[150:151], v[156:157] op_sel_hi:[1,0]
	v_rcp_f32_e32 v148, v148
	v_rcp_f32_e32 v149, v149
	v_rcp_f32_e32 v150, v150
	v_rcp_f32_e32 v151, v151
	v_pk_add_f32 v[24:25], v[24:25], v[156:157] op_sel_hi:[1,0]
	v_pk_add_f32 v[26:27], v[26:27], v[156:157] op_sel_hi:[1,0]
	v_pk_mul_f32 v[28:29], v[28:29], v[148:149]
	v_pk_mul_f32 v[30:31], v[30:31], v[150:151]
	v_pk_mul_f32 v[24:25], v[24:25], v[28:29]
	v_pk_mul_f32 v[26:27], v[26:27], v[30:31]
	v_pk_fma_f32 v[20:21], v[20:21], s[24:25], v[36:37] op_sel_hi:[1,0,1]
	v_pk_fma_f32 v[22:23], v[22:23], s[24:25], v[38:39] op_sel_hi:[1,0,1]
	v_pk_fma_f32 v[16:17], v[16:17], s[24:25], v[104:105] op_sel_hi:[1,0,1]
	v_pk_fma_f32 v[18:19], v[18:19], s[24:25], v[106:107] op_sel_hi:[1,0,1]
	v_min_f32_e32 v20, 0x40e00000, v20
	v_min_f32_e32 v21, 0x40e00000, v21
	v_min_f32_e32 v22, 0x40e00000, v22
	v_min_f32_e32 v23, 0x40e00000, v23
	v_pk_mul_f32 v[148:149], v[20:21], v[144:145] op_sel_hi:[1,0]
	v_pk_mul_f32 v[150:151], v[22:23], v[144:145] op_sel_hi:[1,0]
	v_exp_f32_e32 v148, v148
	v_exp_f32_e32 v149, v149
	v_exp_f32_e32 v150, v150
	v_exp_f32_e32 v151, v151
	v_med3_f32 v16, v16, s75, v154
	v_med3_f32 v17, v17, s75, v154
	v_med3_f32 v18, v18, s75, v154
	v_med3_f32 v19, v19, s75, v154
	v_pk_add_f32 v[148:149], v[148:149], v[156:157] op_sel_hi:[1,0]
	v_pk_add_f32 v[150:151], v[150:151], v[156:157] op_sel_hi:[1,0]
	v_rcp_f32_e32 v148, v148
	v_rcp_f32_e32 v149, v149
	v_rcp_f32_e32 v150, v150
	v_rcp_f32_e32 v151, v151
	v_pk_add_f32 v[16:17], v[16:17], v[156:157] op_sel_hi:[1,0]
	v_pk_add_f32 v[18:19], v[18:19], v[156:157] op_sel_hi:[1,0]
	v_pk_mul_f32 v[20:21], v[20:21], v[148:149]
	v_pk_mul_f32 v[22:23], v[22:23], v[150:151]
	v_pk_mul_f32 v[16:17], v[16:17], v[20:21]
	v_pk_mul_f32 v[18:19], v[18:19], v[22:23]
	v_cvt_pk_fp8_f32 v28, v24, v25
	v_cvt_pk_fp8_f32 v28, v26, v27 op_sel:[0,0,1]
	v_cvt_pk_fp8_f32 v29, v16, v17
	v_cvt_pk_fp8_f32 v29, v18, v19 op_sel:[0,0,1]
	s_add_u32 vcc_lo, s14, 0x50000
	s_addc_u32 vcc_hi, s15, 0
	global_store_dwordx2 v146, v[28:29], vcc
	v_pk_fma_f32 v[12:13], v[12:13], s[24:25], v[120:121] op_sel_hi:[1,0,1]
	v_pk_fma_f32 v[14:15], v[14:15], s[24:25], v[122:123] op_sel_hi:[1,0,1]
	v_pk_fma_f32 v[8:9], v[8:9], s[24:25], v[116:117] op_sel_hi:[1,0,1]
	v_pk_fma_f32 v[10:11], v[10:11], s[24:25], v[118:119] op_sel_hi:[1,0,1]
	v_min_f32_e32 v12, 0x40e00000, v12
	v_min_f32_e32 v13, 0x40e00000, v13
	v_min_f32_e32 v14, 0x40e00000, v14
	v_min_f32_e32 v15, 0x40e00000, v15
	v_pk_mul_f32 v[148:149], v[12:13], v[144:145] op_sel_hi:[1,0]
	v_pk_mul_f32 v[150:151], v[14:15], v[144:145] op_sel_hi:[1,0]
	v_exp_f32_e32 v148, v148
	v_exp_f32_e32 v149, v149
	v_exp_f32_e32 v150, v150
	v_exp_f32_e32 v151, v151
	v_med3_f32 v8, v8, s75, v154
	v_med3_f32 v9, v9, s75, v154
	v_med3_f32 v10, v10, s75, v154
	v_med3_f32 v11, v11, s75, v154
	v_pk_add_f32 v[148:149], v[148:149], v[156:157] op_sel_hi:[1,0]
	v_pk_add_f32 v[150:151], v[150:151], v[156:157] op_sel_hi:[1,0]
	v_rcp_f32_e32 v148, v148
	v_rcp_f32_e32 v149, v149
	v_rcp_f32_e32 v150, v150
	v_rcp_f32_e32 v151, v151
	v_pk_add_f32 v[8:9], v[8:9], v[156:157] op_sel_hi:[1,0]
	v_pk_add_f32 v[10:11], v[10:11], v[156:157] op_sel_hi:[1,0]
	v_pk_mul_f32 v[12:13], v[12:13], v[148:149]
	v_pk_mul_f32 v[14:15], v[14:15], v[150:151]
	v_pk_mul_f32 v[8:9], v[8:9], v[12:13]
	v_pk_mul_f32 v[10:11], v[10:11], v[14:15]
	v_pk_fma_f32 v[4:5], v[4:5], s[24:25], v[36:37] op_sel_hi:[1,0,1]
	v_pk_fma_f32 v[6:7], v[6:7], s[24:25], v[38:39] op_sel_hi:[1,0,1]
	v_pk_fma_f32 v[0:1], v[0:1], s[24:25], v[104:105] op_sel_hi:[1,0,1]
	v_pk_fma_f32 v[2:3], v[2:3], s[24:25], v[106:107] op_sel_hi:[1,0,1]
	v_min_f32_e32 v4, 0x40e00000, v4
	v_min_f32_e32 v5, 0x40e00000, v5
	v_min_f32_e32 v6, 0x40e00000, v6
	v_min_f32_e32 v7, 0x40e00000, v7
	v_pk_mul_f32 v[148:149], v[4:5], v[144:145] op_sel_hi:[1,0]
	v_pk_mul_f32 v[150:151], v[6:7], v[144:145] op_sel_hi:[1,0]
	v_exp_f32_e32 v148, v148
	v_exp_f32_e32 v149, v149
	v_exp_f32_e32 v150, v150
	v_exp_f32_e32 v151, v151
	v_med3_f32 v0, v0, s75, v154
	v_med3_f32 v1, v1, s75, v154
	v_med3_f32 v2, v2, s75, v154
	v_med3_f32 v3, v3, s75, v154
	v_pk_add_f32 v[148:149], v[148:149], v[156:157] op_sel_hi:[1,0]
	v_pk_add_f32 v[150:151], v[150:151], v[156:157] op_sel_hi:[1,0]
	v_rcp_f32_e32 v148, v148
	v_rcp_f32_e32 v149, v149
	v_rcp_f32_e32 v150, v150
	v_rcp_f32_e32 v151, v151
	v_pk_add_f32 v[0:1], v[0:1], v[156:157] op_sel_hi:[1,0]
	v_pk_add_f32 v[2:3], v[2:3], v[156:157] op_sel_hi:[1,0]
	v_pk_mul_f32 v[4:5], v[4:5], v[148:149]
	v_pk_mul_f32 v[6:7], v[6:7], v[150:151]
	v_pk_mul_f32 v[0:1], v[0:1], v[4:5]
	v_pk_mul_f32 v[2:3], v[2:3], v[6:7]
	v_cvt_pk_fp8_f32 v12, v8, v9
	v_cvt_pk_fp8_f32 v12, v10, v11 op_sel:[0,0,1]
	v_cvt_pk_fp8_f32 v13, v0, v1
	v_cvt_pk_fp8_f32 v13, v2, v3 op_sel:[0,0,1]
	s_add_u32 vcc_lo, s14, 0x58000
	s_addc_u32 vcc_hi, s15, 0
	global_store_dwordx2 v146, v[12:13], vcc
	s_and_b64 vcc, exec, s[4:5]
	s_mov_b64 s[4:5], -1
	s_cbranch_vccnz .LBB0_1029
	v_mbcnt_lo_u32_b32 v0, -1, 0
	v_mbcnt_hi_u32_b32 v0, -1, v0
	s_andn2_b64 vcc, exec, s[12:13]
	v_add_u32_e32 v0, s0, v0
	v_lshl_add_u32 v0, v0, 4, 0
	v_add_u32_e32 v0, 0x21000, v0
	ds_read_b128 v[36:39], v0
	s_cbranch_vccnz .LBB0_1028
	s_barrier
	s_branch .LBB0_1028
